# stack10 + prologue int8 weight strips: the 32 gain loads of strip_stage issued in two batches of 16 (were eight serialized groups of 4)
# speedup vs baseline: 1.0012x; 1.0012x over previous
; #define GAS __attribute__((address_space(1)))
; #define LAS __attribute__((address_space(3)))
; __device__ __forceinline__ unsigned pkh2(float lo, float hi) { f32x2_t_ v = {lo, hi}; f16x2_t_ h = __builtin_convertvector(v, f16x2_t_); return __builtin_bit_cast(unsigned, h); }
; __device__ __forceinline__ void strip_stage(LAS unsigned char* lds, const float* gain, int wave, int lane, const float (&v)[4][32]) {
;     const int n = lane & 31, h = lane >> 5;
; #pragma unroll
;     for (int q = 0; q < 4; ++q) { const int kb = 256 * wave + 64 * q + 32 * h;
; #pragma unroll
;         for (int j = 0; j < 4; ++j) { const f32x4 ga = *(const GAS f32x4*)(gain + kb + 8 * j), gb = *(const GAS f32x4*)(gain + kb + 8 * j + 4);
;             v4u o; o.x = pkh2(v[q][8 * j] * ga.x, v[q][8 * j + 1] * ga.y); o.y = pkh2(v[q][8 * j + 2] * ga.z, v[q][8 * j + 3] * ga.w);
;             o.z = pkh2(v[q][8 * j + 4] * gb.x, v[q][8 * j + 5] * gb.y); o.w = pkh2(v[q][8 * j + 6] * gb.z, v[q][8 * j + 7] * gb.w);
;             *(LAS v4u*)(lds + n * SROW + 2 * (kb + 8 * j)) = o; } }
.LBB0_18:
	v_lshl_add_u64 v[14:15], v[22:23], 2, s[34:35]
	global_load_dwordx4 v[2:5], v[14:15], off offset:48
	global_load_dwordx4 v[6:9], v[14:15], off offset:32
	global_load_dwordx4 v[10:13], v[14:15], off offset:16
	global_load_dwordx4 v[166:169], v[14:15], off
	global_load_dwordx4 v[176:179], v[14:15], off offset:112
	global_load_dwordx4 v[180:183], v[14:15], off offset:96
	global_load_dwordx4 v[184:187], v[14:15], off offset:80
	global_load_dwordx4 v[188:191], v[14:15], off offset:64
	global_load_dwordx4 v[192:195], v[14:15], off offset:304
	global_load_dwordx4 v[196:199], v[14:15], off offset:288
	global_load_dwordx4 v[200:203], v[14:15], off offset:272
	global_load_dwordx4 v[204:207], v[14:15], off offset:256
	global_load_dwordx4 v[208:211], v[14:15], off offset:368
	global_load_dwordx4 v[212:215], v[14:15], off offset:352
	global_load_dwordx4 v[216:219], v[14:15], off offset:336
	global_load_dwordx4 v[220:223], v[14:15], off offset:320
	v_add_u32_e32 v154, v158, v159
	s_add_i32 s53, s53, s88
	s_cmpk_gt_i32 s53, 0xaff
	s_cselect_b64 s[6:7], -1, 0
	s_mov_b64 s[8:9], 0
	s_and_b64 vcc, exec, s[6:7]
	s_mov_b64 s[10:11], 0
	s_mov_b64 s[34:35], 0
	s_waitcnt vmcnt(15)
	v_pk_mul_f32 v[2:3], v[30:31], v[2:3]
	s_waitcnt vmcnt(14)
	v_pk_mul_f32 v[6:7], v[26:27], v[6:7]
	s_waitcnt vmcnt(13)
	v_pk_mul_f32 v[10:11], v[82:83], v[10:11]
	s_waitcnt vmcnt(12)
	v_pk_mul_f32 v[16:17], v[76:77], v[166:167]
	v_pk_mul_f32 v[8:9], v[28:29], v[8:9]
	v_cvt_pk_f16_f32 v166, v16, v17
	v_pk_mul_f32 v[16:17], v[78:79], v[168:169]
	v_cvt_pk_f16_f32 v168, v10, v11
	v_pk_mul_f32 v[10:11], v[84:85], v[12:13]
	v_cvt_pk_f16_f32 v6, v6, v7
	v_cvt_pk_f16_f32 v7, v8, v9
	v_cvt_pk_f16_f32 v8, v2, v3
	v_pk_mul_f32 v[2:3], v[32:33], v[4:5]
	v_cvt_pk_f16_f32 v167, v16, v17
	v_cvt_pk_f16_f32 v169, v10, v11
	v_cvt_pk_f16_f32 v9, v2, v3
	ds_write_b128 v154, v[166:169]
	ds_write_b128 v154, v[6:9] offset:16
	s_waitcnt vmcnt(11)
	v_pk_mul_f32 v[2:3], v[46:47], v[176:177]
	s_waitcnt vmcnt(10)
	v_pk_mul_f32 v[6:7], v[42:43], v[180:181]
	s_waitcnt vmcnt(9)
	v_pk_mul_f32 v[10:11], v[38:39], v[184:185]
	s_waitcnt vmcnt(8)
	v_pk_mul_f32 v[16:17], v[34:35], v[188:189]
	v_pk_mul_f32 v[8:9], v[44:45], v[182:183]
	v_cvt_pk_f16_f32 v166, v16, v17
	v_pk_mul_f32 v[16:17], v[36:37], v[190:191]
	v_cvt_pk_f16_f32 v168, v10, v11
	v_pk_mul_f32 v[10:11], v[40:41], v[186:187]
	v_cvt_pk_f16_f32 v6, v6, v7
	v_cvt_pk_f16_f32 v7, v8, v9
	v_cvt_pk_f16_f32 v8, v2, v3
	v_pk_mul_f32 v[2:3], v[48:49], v[178:179]
	v_cvt_pk_f16_f32 v167, v16, v17
	v_cvt_pk_f16_f32 v169, v10, v11
	v_cvt_pk_f16_f32 v9, v2, v3
	ds_write_b128 v154, v[166:169] offset:32
	ds_write_b128 v154, v[6:9] offset:48
	s_waitcnt vmcnt(7)
	v_pk_mul_f32 v[2:3], v[62:63], v[192:193]
	s_waitcnt vmcnt(6)
	v_pk_mul_f32 v[6:7], v[58:59], v[196:197]
	s_waitcnt vmcnt(5)
	v_pk_mul_f32 v[10:11], v[54:55], v[200:201]
	s_waitcnt vmcnt(4)
	v_pk_mul_f32 v[16:17], v[50:51], v[204:205]
	v_pk_mul_f32 v[8:9], v[60:61], v[198:199]
	v_cvt_pk_f16_f32 v166, v16, v17
	v_pk_mul_f32 v[16:17], v[52:53], v[206:207]
	v_cvt_pk_f16_f32 v168, v10, v11
	v_pk_mul_f32 v[10:11], v[56:57], v[202:203]
	v_cvt_pk_f16_f32 v6, v6, v7
	v_cvt_pk_f16_f32 v7, v8, v9
	v_cvt_pk_f16_f32 v8, v2, v3
	v_pk_mul_f32 v[2:3], v[64:65], v[194:195]
	v_cvt_pk_f16_f32 v167, v16, v17
	v_cvt_pk_f16_f32 v169, v10, v11
	v_cvt_pk_f16_f32 v9, v2, v3
	ds_write_b128 v160, v[166:169]
	ds_write_b128 v154, v[6:9] offset:144
	s_waitcnt vmcnt(3)
	v_pk_mul_f32 v[2:3], v[86:87], v[208:209]
	s_waitcnt vmcnt(2)
	v_pk_mul_f32 v[6:7], v[74:75], v[212:213]
	s_waitcnt vmcnt(1)
	v_pk_mul_f32 v[10:11], v[70:71], v[216:217]
	s_waitcnt vmcnt(0)
	v_pk_mul_f32 v[16:17], v[66:67], v[220:221]
	v_pk_mul_f32 v[8:9], v[80:81], v[214:215]
	v_cvt_pk_f16_f32 v166, v16, v17
	v_pk_mul_f32 v[16:17], v[68:69], v[222:223]
	v_cvt_pk_f16_f32 v168, v10, v11
	v_pk_mul_f32 v[10:11], v[72:73], v[218:219]
	v_cvt_pk_f16_f32 v6, v6, v7
	v_cvt_pk_f16_f32 v7, v8, v9
	v_cvt_pk_f16_f32 v8, v2, v3
	v_pk_mul_f32 v[2:3], v[88:89], v[210:211]
	v_cvt_pk_f16_f32 v167, v16, v17
	v_cvt_pk_f16_f32 v169, v10, v11
	v_cvt_pk_f16_f32 v9, v2, v3
	ds_write_b128 v154, v[166:169] offset:160
	ds_write_b128 v154, v[6:9] offset:176
	global_load_dwordx4 v[2:5], v[14:15], off offset:560
	global_load_dwordx4 v[6:9], v[14:15], off offset:544
	global_load_dwordx4 v[10:13], v[14:15], off offset:528
	global_load_dwordx4 v[166:169], v[14:15], off offset:512
	global_load_dwordx4 v[176:179], v[14:15], off offset:624
	global_load_dwordx4 v[180:183], v[14:15], off offset:608
	global_load_dwordx4 v[184:187], v[14:15], off offset:592
	global_load_dwordx4 v[188:191], v[14:15], off offset:576
	global_load_dwordx4 v[192:195], v[14:15], off offset:816
	global_load_dwordx4 v[196:199], v[14:15], off offset:800
	global_load_dwordx4 v[200:203], v[14:15], off offset:784
	global_load_dwordx4 v[204:207], v[14:15], off offset:768
	global_load_dwordx4 v[208:211], v[14:15], off offset:880
	global_load_dwordx4 v[212:215], v[14:15], off offset:864
	global_load_dwordx4 v[216:219], v[14:15], off offset:848
	global_load_dwordx4 v[220:223], v[14:15], off offset:832
	s_waitcnt vmcnt(15)
	v_pk_mul_f32 v[2:3], v[102:103], v[2:3]
	s_waitcnt vmcnt(14)
; #define GAS __attribute__((address_space(1)))
; #define LAS __attribute__((address_space(3)))
; __device__ __forceinline__ unsigned pkh2(float lo, float hi) { f32x2_t_ v = {lo, hi}; f16x2_t_ h = __builtin_convertvector(v, f16x2_t_); return __builtin_bit_cast(unsigned, h); }
; __device__ __forceinline__ void strip_stage(LAS unsigned char* lds, const float* gain, int wave, int lane, const float (&v)[4][32]) {
;     const int n = lane & 31, h = lane >> 5;
; #pragma unroll
;     for (int q = 0; q < 4; ++q) { const int kb = 256 * wave + 64 * q + 32 * h;
; #pragma unroll
;         for (int j = 0; j < 4; ++j) { const f32x4 ga = *(const GAS f32x4*)(gain + kb + 8 * j), gb = *(const GAS f32x4*)(gain + kb + 8 * j + 4);
;             v4u o; o.x = pkh2(v[q][8 * j] * ga.x, v[q][8 * j + 1] * ga.y); o.y = pkh2(v[q][8 * j + 2] * ga.z, v[q][8 * j + 3] * ga.w);
;             o.z = pkh2(v[q][8 * j + 4] * gb.x, v[q][8 * j + 5] * gb.y); o.w = pkh2(v[q][8 * j + 6] * gb.z, v[q][8 * j + 7] * gb.w);
;             *(LAS v4u*)(lds + n * SROW + 2 * (kb + 8 * j)) = o; } }
; __global__ void __launch_bounds__(NWAVES * 64, 2) fwd(Args args) {
;     ...
;           while (s < NS_ALL) {
;               strip_stage(lds, cg_, wave, lane, v_);
;               __syncthreads();
;               const int nx_ = s + G; unsigned char* nd_ = nullptr; float* nc_ = nullptr; const float* ng_ = nullptr;
;               if (nx_ < NS_ALL) { STRIP_RESOLVE(nx_, cw_, cn_, c0_, ng_, nd_, nc_); strip_load(cw_, cn_, c0_, wave, lane, v_); }
	v_pk_mul_f32 v[6:7], v[98:99], v[6:7]
	s_waitcnt vmcnt(13)
	v_pk_mul_f32 v[10:11], v[94:95], v[10:11]
	s_waitcnt vmcnt(12)
	v_pk_mul_f32 v[16:17], v[90:91], v[166:167]
	v_pk_mul_f32 v[8:9], v[100:101], v[8:9]
	v_cvt_pk_f16_f32 v166, v16, v17
	v_pk_mul_f32 v[16:17], v[92:93], v[168:169]
	v_cvt_pk_f16_f32 v168, v10, v11
	v_pk_mul_f32 v[10:11], v[96:97], v[12:13]
	v_cvt_pk_f16_f32 v6, v6, v7
	v_cvt_pk_f16_f32 v7, v8, v9
	v_cvt_pk_f16_f32 v8, v2, v3
	v_pk_mul_f32 v[2:3], v[104:105], v[4:5]
	v_cvt_pk_f16_f32 v167, v16, v17
	v_cvt_pk_f16_f32 v169, v10, v11
	v_cvt_pk_f16_f32 v9, v2, v3
	ds_write_b128 v161, v[166:169]
	ds_write_b128 v154, v[6:9] offset:272
	s_waitcnt vmcnt(11)
	v_pk_mul_f32 v[2:3], v[118:119], v[176:177]
	s_waitcnt vmcnt(10)
	v_pk_mul_f32 v[6:7], v[114:115], v[180:181]
	s_waitcnt vmcnt(9)
	v_pk_mul_f32 v[10:11], v[110:111], v[184:185]
	s_waitcnt vmcnt(8)
	v_pk_mul_f32 v[16:17], v[106:107], v[188:189]
	v_pk_mul_f32 v[8:9], v[116:117], v[182:183]
	v_cvt_pk_f16_f32 v166, v16, v17
	v_pk_mul_f32 v[16:17], v[108:109], v[190:191]
	v_cvt_pk_f16_f32 v168, v10, v11
	v_pk_mul_f32 v[10:11], v[112:113], v[186:187]
	v_cvt_pk_f16_f32 v6, v6, v7
	v_cvt_pk_f16_f32 v7, v8, v9
	v_cvt_pk_f16_f32 v8, v2, v3
	v_pk_mul_f32 v[2:3], v[120:121], v[178:179]
	v_cvt_pk_f16_f32 v167, v16, v17
	v_cvt_pk_f16_f32 v169, v10, v11
	v_cvt_pk_f16_f32 v9, v2, v3
	ds_write_b128 v154, v[166:169] offset:288
	ds_write_b128 v154, v[6:9] offset:304
	s_waitcnt vmcnt(7)
	v_pk_mul_f32 v[2:3], v[134:135], v[192:193]
	s_waitcnt vmcnt(6)
	v_pk_mul_f32 v[6:7], v[130:131], v[196:197]
	s_waitcnt vmcnt(5)
	v_pk_mul_f32 v[10:11], v[126:127], v[200:201]
	s_waitcnt vmcnt(4)
	v_pk_mul_f32 v[16:17], v[122:123], v[204:205]
	v_pk_mul_f32 v[8:9], v[132:133], v[198:199]
	v_cvt_pk_f16_f32 v166, v16, v17
	v_pk_mul_f32 v[16:17], v[124:125], v[206:207]
	v_cvt_pk_f16_f32 v168, v10, v11
	v_pk_mul_f32 v[10:11], v[128:129], v[202:203]
	v_cvt_pk_f16_f32 v6, v6, v7
	v_cvt_pk_f16_f32 v7, v8, v9
	v_cvt_pk_f16_f32 v8, v2, v3
	v_pk_mul_f32 v[2:3], v[136:137], v[194:195]
	v_cvt_pk_f16_f32 v167, v16, v17
	v_cvt_pk_f16_f32 v169, v10, v11
	v_cvt_pk_f16_f32 v9, v2, v3
	ds_write_b128 v162, v[166:169]
	ds_write_b128 v154, v[6:9] offset:400
	s_nop 0
	s_waitcnt vmcnt(3)
	v_pk_mul_f32 v[2:3], v[150:151], v[208:209]
	s_waitcnt vmcnt(2)
	v_pk_mul_f32 v[6:7], v[146:147], v[212:213]
	s_waitcnt vmcnt(1)
	v_pk_mul_f32 v[10:11], v[142:143], v[216:217]
	s_waitcnt vmcnt(0)
	v_pk_mul_f32 v[14:15], v[138:139], v[220:221]
	v_pk_mul_f32 v[16:17], v[140:141], v[222:223]
	v_pk_mul_f32 v[8:9], v[148:149], v[214:215]
	v_cvt_pk_f16_f32 v14, v14, v15
	v_cvt_pk_f16_f32 v15, v16, v17
	v_cvt_pk_f16_f32 v16, v10, v11
	v_pk_mul_f32 v[10:11], v[144:145], v[218:219]
	v_cvt_pk_f16_f32 v6, v6, v7
	v_cvt_pk_f16_f32 v7, v8, v9
	v_cvt_pk_f16_f32 v8, v2, v3
	v_pk_mul_f32 v[2:3], v[152:153], v[210:211]
	v_cvt_pk_f16_f32 v17, v10, v11
	v_cvt_pk_f16_f32 v9, v2, v3
	ds_write_b128 v154, v[14:17] offset:416
	ds_write_b128 v154, v[6:9] offset:432
	v_mov_b32_e32 v12, v218
	v_mov_b32_e32 v13, v219
	v_mov_b32_e32 v4, v210
	v_mov_b32_e32 v5, v211
	s_waitcnt lgkmcnt(0)
	s_barrier
	s_cbranch_vccnz .LBB0_24
	s_mul_hi_i32 s8, s53, 0x2e8ba2e9
	s_lshr_b32 s9, s8, 31
	s_ashr_i32 s8, s8, 7
	s_add_i32 s38, s8, s9
	s_mul_i32 s8, s38, 0xfffffd40
	s_add_i32 s37, s53, s8
	s_mul_i32 s8, s38, 0xffffa800
	s_ashr_i32 s39, s38, 31
	s_add_i32 s36, s44, s8
	s_cmpk_gt_i32 s37, 0x1bf
	s_mov_b64 s[40:41], -1
	s_cbranch_scc0 .LBB0_21
	v_readlane_b32 s56, v250, 34
	s_lshl_b64 s[8:9], s[38:39], 26
	v_readlane_b32 s66, v250, 44
	v_readlane_b32 s67, v250, 45
	s_add_u32 s12, s66, s8
	v_readlane_b32 s57, v250, 35
	v_readlane_b32 s58, v250, 36
	v_readlane_b32 s59, v250, 37
	v_readlane_b32 s60, v250, 38
	v_readlane_b32 s61, v250, 39
	v_readlane_b32 s62, v250, 40
	v_readlane_b32 s63, v250, 41
	v_readlane_b32 s64, v250, 42
	v_readlane_b32 s65, v250, 43
	v_readlane_b32 s68, v250, 46
	v_readlane_b32 s69, v250, 47
	v_readlane_b32 s70, v250, 48
	v_readlane_b32 s71, v250, 49
	s_addc_u32 s13, s67, s9
	s_lshl_b32 s8, s38, 11
	s_ashr_i32 s9, s8, 31
	v_readlane_b32 s56, v250, 2
	s_add_i32 s16, s36, 0xffffc800
	s_lshl_b64 s[8:9], s[8:9], 2
	v_readlane_b32 s64, v250, 10
	v_readlane_b32 s65, v250, 11
	s_add_u32 s34, s64, s8
	s_addc_u32 s35, s65, s9
	s_lshl_b64 s[8:9], s[38:39], 24
	s_lshl_b64 s[10:11], s[16:17], 11
	v_readlane_b32 s39, v250, 28
	s_add_u32 s8, s39, s8
	v_readlane_b32 s39, v250, 29
	s_addc_u32 s9, s39, s9
	s_add_u32 s8, s8, s10
	s_addc_u32 s9, s9, s11
	s_lshl_b32 s10, s38, 13
	s_ashr_i32 s11, s10, 31
	s_lshl_b64 s[10:11], s[10:11], 2
	v_readlane_b32 s39, v250, 32
	s_add_u32 s39, s39, s10
	v_readlane_b32 s10, v250, 33
	s_addc_u32 s40, s10, s11
	s_lshl_b64 s[10:11], s[16:17], 2
	s_add_u32 s10, s39, s10
	v_readlane_b32 s57, v250, 3
	v_readlane_b32 s58, v250, 4
	v_readlane_b32 s59, v250, 5
	v_readlane_b32 s60, v250, 6
	v_readlane_b32 s61, v250, 7
	v_readlane_b32 s62, v250, 8
	v_readlane_b32 s63, v250, 9
	v_readlane_b32 s66, v250, 12
	v_readlane_b32 s67, v250, 13
	v_readlane_b32 s68, v250, 14
	v_readlane_b32 s69, v250, 15
	v_readlane_b32 s70, v250, 16
	v_readlane_b32 s71, v250, 17
	s_addc_u32 s11, s40, s11
	s_mov_b64 s[40:41], 0
